# W_out epilogue rewritten: all x/stats loads of a column half issued up front with counted vmcnt waits (was one HBM round trip per row)
# baseline (speedup 1.0000x reference)
; #define GAS __attribute__((address_space(1)))
; #define LAS __attribute__((address_space(3)))
; __device__ __forceinline__ v4u pack8(const f32x4 a, const f32x4 b) { v4u w; w.x = cvt_pk_bf16(a[0], a[1]); w.y = cvt_pk_bf16(a[2], a[3]); w.z = cvt_pk_bf16(b[0], b[1]); w.w = cvt_pk_bf16(b[2], b[3]); return w; }
; #define EPI_LOOP_AM for (int ai = 0; ai < 2; ++ai) _Pragma("unroll") for (int m = 0; m < 4; ++m)
;     __device__ __forceinline__ void operator()(Acc& acc, const Unit& u, LAS unsigned char*, int wr, int wc, int fr, int fq) const {
;         const int colb = u.p1 * 256 + wc * 32 + 8 * fq;
; #pragma unroll
;         for (int bj = 0; bj < 2; ++bj) { const int col = colb + bj * 128;
;             const f32x4 ga = *(const GAS f32x4*)(g0 + col), gb = *(const GAS f32x4*)(g0 + col + 4), ba = *(const GAS f32x4*)(b0 + col), bb = *(const GAS f32x4*)(b0 + col + 4);
; #pragma unroll
;             EPI_LOOP_AM { const int row = u.p0 * 256 + 128 * ai + 64 * wr + 16 * m + fr; const f32x2 st = *(const GAS f32x2*)(st0 + 2 * row); const size_t off = (size_t)row * D + col;
;                 const f32x4 xa = *(const GAS f32x4*)(x + off), xb = *(const GAS f32x4*)(x + off + 4);
;                 *(GAS v4u*)(z1 + off) = pack8(((xa - st.x) * st.y * ga + ba) * ALPHA + acc[ai][bj][m][0], ((xb - st.x) * st.y * gb + bb) * ALPHA + acc[ai][bj][m][1]); } }
;     }
.LBB0_1325:
	s_lshl_b32 s1, s92, 8
	s_or_b32 s1, s1, s80
	s_andn2_b64 vcc, exec, s[60:61]
	v_lshl_add_u32 v146, v171, 3, s1
	s_lshl_b32 s1, s62, 8
	s_add_i32 s1, s1, s78
	v_add_u32_e32 v164, s1, v170
	s_mov_b64 s[60:61], -1
	v_lshl_add_u32 v158, v164, 11, v146
	v_lshlrev_b32_e32 v160, 3, v164
	v_lshlrev_b32_e32 v161, 2, v146
	v_lshlrev_b32_e32 v159, 1, v158
	v_lshlrev_b32_e32 v158, 2, v158
	global_load_dwordx4 v[136:139], v161, s[14:15]
	global_load_dwordx4 v[128:131], v161, s[14:15] offset:16
	global_load_dwordx4 v[132:135], v161, s[16:17]
	global_load_dwordx4 v[140:143], v161, s[16:17] offset:16
	global_load_dwordx2 v[182:183], v160, s[40:41]
	global_load_dwordx4 v[196:199], v158, s[12:13]
	global_load_dwordx4 v[200:203], v158, s[12:13] offset:16
	s_add_u32 s98, s12, 0x20000
	s_addc_u32 s99, s13, 0
	global_load_dwordx2 v[184:185], v160, s[40:41] offset:128
	global_load_dwordx4 v[204:207], v158, s[98:99]
	global_load_dwordx4 v[208:211], v158, s[98:99] offset:16
	s_add_u32 s98, s12, 0x40000
	s_addc_u32 s99, s13, 0
	global_load_dwordx2 v[186:187], v160, s[40:41] offset:256
	global_load_dwordx4 v[212:215], v158, s[98:99]
	global_load_dwordx4 v[216:219], v158, s[98:99] offset:16
	s_add_u32 s98, s12, 0x60000
	s_addc_u32 s99, s13, 0
	global_load_dwordx2 v[148:149], v160, s[40:41] offset:384
	global_load_dwordx4 v[220:223], v158, s[98:99]
	global_load_dwordx4 v[224:227], v158, s[98:99] offset:16
	s_add_u32 s98, s12, 0x100000
	s_addc_u32 s99, s13, 0
	global_load_dwordx2 v[150:151], v160, s[40:41] offset:1024
	global_load_dwordx4 v[228:231], v158, s[98:99]
	global_load_dwordx4 v[232:235], v158, s[98:99] offset:16
	s_add_u32 s98, s12, 0x120000
	s_addc_u32 s99, s13, 0
	global_load_dwordx2 v[152:153], v160, s[40:41] offset:1152
	global_load_dwordx4 v[236:239], v158, s[98:99]
	global_load_dwordx4 v[240:243], v158, s[98:99] offset:16
	s_add_u32 s98, s12, 0x140000
	s_addc_u32 s99, s13, 0
	global_load_dwordx2 v[154:155], v160, s[40:41] offset:1280
	global_load_dwordx4 v[244:247], v158, s[98:99]
	global_load_dwordx4 v[248:251], v158, s[98:99] offset:16
	s_add_u32 s98, s12, 0x160000
	s_addc_u32 s99, s13, 0
	global_load_dwordx2 v[156:157], v160, s[40:41] offset:1408
	global_load_dwordx4 v[174:177], v158, s[98:99]
	global_load_dwordx4 v[178:181], v158, s[98:99] offset:16
	s_waitcnt vmcnt(21)
	v_sub_f32_e32 v196, v196, v182
	v_sub_f32_e32 v197, v197, v182
	v_sub_f32_e32 v198, v198, v182
	v_sub_f32_e32 v199, v199, v182
	v_sub_f32_e32 v200, v200, v182
	v_sub_f32_e32 v201, v201, v182
	v_sub_f32_e32 v202, v202, v182
	v_sub_f32_e32 v203, v203, v182
	v_pk_mul_f32 v[196:197], v[182:183], v[196:197] op_sel:[1,0]
	v_pk_mul_f32 v[198:199], v[182:183], v[198:199] op_sel:[1,0]
	v_pk_mul_f32 v[200:201], v[182:183], v[200:201] op_sel:[1,0]
	v_pk_mul_f32 v[202:203], v[182:183], v[202:203] op_sel:[1,0]
	v_pk_fma_f32 v[196:197], v[136:137], v[196:197], v[132:133]
	v_pk_fma_f32 v[198:199], v[138:139], v[198:199], v[134:135]
	v_pk_fma_f32 v[200:201], v[128:129], v[200:201], v[140:141]
	v_pk_fma_f32 v[202:203], v[130:131], v[202:203], v[142:143]
	v_pk_fma_f32 v[124:125], v[196:197], s[50:51], v[124:125] op_sel_hi:[1,0,1]
	v_pk_fma_f32 v[126:127], v[198:199], s[50:51], v[126:127] op_sel_hi:[1,0,1]
	v_pk_fma_f32 v[120:121], v[200:201], s[50:51], v[120:121] op_sel_hi:[1,0,1]
	v_pk_fma_f32 v[122:123], v[202:203], s[50:51], v[122:123] op_sel_hi:[1,0,1]
	v_cvt_pk_bf16_f32 v196, v124, v125
	v_cvt_pk_bf16_f32 v197, v126, v127
	v_cvt_pk_bf16_f32 v198, v120, v121
	v_cvt_pk_bf16_f32 v199, v122, v123
	global_store_dwordx4 v159, v[196:199], s[38:39]
	s_waitcnt vmcnt(19)
	v_sub_f32_e32 v204, v204, v184
	v_sub_f32_e32 v205, v205, v184
	v_sub_f32_e32 v206, v206, v184
	v_sub_f32_e32 v207, v207, v184
	v_sub_f32_e32 v208, v208, v184
	v_sub_f32_e32 v209, v209, v184
	v_sub_f32_e32 v210, v210, v184
	v_sub_f32_e32 v211, v211, v184
	v_pk_mul_f32 v[204:205], v[184:185], v[204:205] op_sel:[1,0]
	v_pk_mul_f32 v[206:207], v[184:185], v[206:207] op_sel:[1,0]
	v_pk_mul_f32 v[208:209], v[184:185], v[208:209] op_sel:[1,0]
	v_pk_mul_f32 v[210:211], v[184:185], v[210:211] op_sel:[1,0]
	v_pk_fma_f32 v[204:205], v[136:137], v[204:205], v[132:133]
	v_pk_fma_f32 v[206:207], v[138:139], v[206:207], v[134:135]
	v_pk_fma_f32 v[208:209], v[128:129], v[208:209], v[140:141]
	v_pk_fma_f32 v[210:211], v[130:131], v[210:211], v[142:143]
	v_pk_fma_f32 v[116:117], v[204:205], s[50:51], v[116:117] op_sel_hi:[1,0,1]
	v_pk_fma_f32 v[118:119], v[206:207], s[50:51], v[118:119] op_sel_hi:[1,0,1]
	v_pk_fma_f32 v[112:113], v[208:209], s[50:51], v[112:113] op_sel_hi:[1,0,1]
	v_pk_fma_f32 v[114:115], v[210:211], s[50:51], v[114:115] op_sel_hi:[1,0,1]
	v_cvt_pk_bf16_f32 v204, v116, v117
	v_cvt_pk_bf16_f32 v205, v118, v119
	v_cvt_pk_bf16_f32 v206, v112, v113
	v_cvt_pk_bf16_f32 v207, v114, v115
	s_add_u32 s100, s38, 0x10000
	s_addc_u32 s101, s39, 0
	global_store_dwordx4 v159, v[204:207], s[100:101]
	s_waitcnt vmcnt(17)
	v_sub_f32_e32 v212, v212, v186
	v_sub_f32_e32 v213, v213, v186
	v_sub_f32_e32 v214, v214, v186
	v_sub_f32_e32 v215, v215, v186
	v_sub_f32_e32 v216, v216, v186
	v_sub_f32_e32 v217, v217, v186
	v_sub_f32_e32 v218, v218, v186
	v_sub_f32_e32 v219, v219, v186
	v_pk_mul_f32 v[212:213], v[186:187], v[212:213] op_sel:[1,0]
	v_pk_mul_f32 v[214:215], v[186:187], v[214:215] op_sel:[1,0]
	v_pk_mul_f32 v[216:217], v[186:187], v[216:217] op_sel:[1,0]
	v_pk_mul_f32 v[218:219], v[186:187], v[218:219] op_sel:[1,0]
	v_pk_fma_f32 v[212:213], v[136:137], v[212:213], v[132:133]
	v_pk_fma_f32 v[214:215], v[138:139], v[214:215], v[134:135]
	v_pk_fma_f32 v[216:217], v[128:129], v[216:217], v[140:141]
	v_pk_fma_f32 v[218:219], v[130:131], v[218:219], v[142:143]
	v_pk_fma_f32 v[108:109], v[212:213], s[50:51], v[108:109] op_sel_hi:[1,0,1]
	v_pk_fma_f32 v[110:111], v[214:215], s[50:51], v[110:111] op_sel_hi:[1,0,1]
	v_pk_fma_f32 v[104:105], v[216:217], s[50:51], v[104:105] op_sel_hi:[1,0,1]
	v_pk_fma_f32 v[106:107], v[218:219], s[50:51], v[106:107] op_sel_hi:[1,0,1]
	v_cvt_pk_bf16_f32 v212, v108, v109
	v_cvt_pk_bf16_f32 v213, v110, v111
	v_cvt_pk_bf16_f32 v214, v104, v105
	v_cvt_pk_bf16_f32 v215, v106, v107
	s_add_u32 s100, s38, 0x20000
	s_addc_u32 s101, s39, 0
	global_store_dwordx4 v159, v[212:215], s[100:101]
	s_waitcnt vmcnt(15)
; #define GAS __attribute__((address_space(1)))
; __device__ __forceinline__ v4u pack8(const f32x4 a, const f32x4 b) { v4u w; w.x = cvt_pk_bf16(a[0], a[1]); w.y = cvt_pk_bf16(a[2], a[3]); w.z = cvt_pk_bf16(b[0], b[1]); w.w = cvt_pk_bf16(b[2], b[3]); return w; }
; #define EPI_LOOP_AM for (int ai = 0; ai < 2; ++ai) _Pragma("unroll") for (int m = 0; m < 4; ++m)
;     __device__ __forceinline__ void operator()(Acc& acc, const Unit& u, LAS unsigned char*, int wr, int wc, int fr, int fq) const {
;     ...
;             const f32x4 ga = *(const GAS f32x4*)(g0 + col), gb = *(const GAS f32x4*)(g0 + col + 4), ba = *(const GAS f32x4*)(b0 + col), bb = *(const GAS f32x4*)(b0 + col + 4);
; #pragma unroll
;             EPI_LOOP_AM { const int row = u.p0 * 256 + 128 * ai + 64 * wr + 16 * m + fr; const f32x2 st = *(const GAS f32x2*)(st0 + 2 * row); const size_t off = (size_t)row * D + col;
;                 const f32x4 xa = *(const GAS f32x4*)(x + off), xb = *(const GAS f32x4*)(x + off + 4);
;                 *(GAS v4u*)(z1 + off) = pack8(((xa - st.x) * st.y * ga + ba) * ALPHA + acc[ai][bj][m][0], ((xb - st.x) * st.y * gb + bb) * ALPHA + acc[ai][bj][m][1]); } }
	v_sub_f32_e32 v220, v220, v148
	v_sub_f32_e32 v221, v221, v148
	v_sub_f32_e32 v222, v222, v148
	v_sub_f32_e32 v223, v223, v148
	v_sub_f32_e32 v224, v224, v148
	v_sub_f32_e32 v225, v225, v148
	v_sub_f32_e32 v226, v226, v148
	v_sub_f32_e32 v227, v227, v148
	v_pk_mul_f32 v[220:221], v[148:149], v[220:221] op_sel:[1,0]
	v_pk_mul_f32 v[222:223], v[148:149], v[222:223] op_sel:[1,0]
	v_pk_mul_f32 v[224:225], v[148:149], v[224:225] op_sel:[1,0]
	v_pk_mul_f32 v[226:227], v[148:149], v[226:227] op_sel:[1,0]
	v_pk_fma_f32 v[220:221], v[136:137], v[220:221], v[132:133]
	v_pk_fma_f32 v[222:223], v[138:139], v[222:223], v[134:135]
	v_pk_fma_f32 v[224:225], v[128:129], v[224:225], v[140:141]
	v_pk_fma_f32 v[226:227], v[130:131], v[226:227], v[142:143]
	v_pk_fma_f32 v[100:101], v[220:221], s[50:51], v[100:101] op_sel_hi:[1,0,1]
	v_pk_fma_f32 v[102:103], v[222:223], s[50:51], v[102:103] op_sel_hi:[1,0,1]
	v_pk_fma_f32 v[96:97], v[224:225], s[50:51], v[96:97] op_sel_hi:[1,0,1]
	v_pk_fma_f32 v[98:99], v[226:227], s[50:51], v[98:99] op_sel_hi:[1,0,1]
	v_cvt_pk_bf16_f32 v220, v100, v101
	v_cvt_pk_bf16_f32 v221, v102, v103
	v_cvt_pk_bf16_f32 v222, v96, v97
	v_cvt_pk_bf16_f32 v223, v98, v99
	s_add_u32 s100, s38, 0x30000
	s_addc_u32 s101, s39, 0
	global_store_dwordx4 v159, v[220:223], s[100:101]
	s_waitcnt vmcnt(13)
	v_sub_f32_e32 v228, v228, v150
	v_sub_f32_e32 v229, v229, v150
	v_sub_f32_e32 v230, v230, v150
	v_sub_f32_e32 v231, v231, v150
	v_sub_f32_e32 v232, v232, v150
	v_sub_f32_e32 v233, v233, v150
	v_sub_f32_e32 v234, v234, v150
	v_sub_f32_e32 v235, v235, v150
	v_pk_mul_f32 v[228:229], v[150:151], v[228:229] op_sel:[1,0]
	v_pk_mul_f32 v[230:231], v[150:151], v[230:231] op_sel:[1,0]
	v_pk_mul_f32 v[232:233], v[150:151], v[232:233] op_sel:[1,0]
	v_pk_mul_f32 v[234:235], v[150:151], v[234:235] op_sel:[1,0]
	v_pk_fma_f32 v[228:229], v[136:137], v[228:229], v[132:133]
	v_pk_fma_f32 v[230:231], v[138:139], v[230:231], v[134:135]
	v_pk_fma_f32 v[232:233], v[128:129], v[232:233], v[140:141]
	v_pk_fma_f32 v[234:235], v[130:131], v[234:235], v[142:143]
	v_pk_fma_f32 v[92:93], v[228:229], s[50:51], v[92:93] op_sel_hi:[1,0,1]
	v_pk_fma_f32 v[94:95], v[230:231], s[50:51], v[94:95] op_sel_hi:[1,0,1]
	v_pk_fma_f32 v[88:89], v[232:233], s[50:51], v[88:89] op_sel_hi:[1,0,1]
	v_pk_fma_f32 v[90:91], v[234:235], s[50:51], v[90:91] op_sel_hi:[1,0,1]
	v_cvt_pk_bf16_f32 v228, v92, v93
	v_cvt_pk_bf16_f32 v229, v94, v95
	v_cvt_pk_bf16_f32 v230, v88, v89
	v_cvt_pk_bf16_f32 v231, v90, v91
	s_add_u32 s100, s38, 0x80000
	s_addc_u32 s101, s39, 0
	global_store_dwordx4 v159, v[228:231], s[100:101]
	s_waitcnt vmcnt(11)
	v_sub_f32_e32 v236, v236, v152
	v_sub_f32_e32 v237, v237, v152
	v_sub_f32_e32 v238, v238, v152
	v_sub_f32_e32 v239, v239, v152
	v_sub_f32_e32 v240, v240, v152
	v_sub_f32_e32 v241, v241, v152
	v_sub_f32_e32 v242, v242, v152
	v_sub_f32_e32 v243, v243, v152
	v_pk_mul_f32 v[236:237], v[152:153], v[236:237] op_sel:[1,0]
	v_pk_mul_f32 v[238:239], v[152:153], v[238:239] op_sel:[1,0]
	v_pk_mul_f32 v[240:241], v[152:153], v[240:241] op_sel:[1,0]
	v_pk_mul_f32 v[242:243], v[152:153], v[242:243] op_sel:[1,0]
	v_pk_fma_f32 v[236:237], v[136:137], v[236:237], v[132:133]
	v_pk_fma_f32 v[238:239], v[138:139], v[238:239], v[134:135]
	v_pk_fma_f32 v[240:241], v[128:129], v[240:241], v[140:141]
	v_pk_fma_f32 v[242:243], v[130:131], v[242:243], v[142:143]
	v_pk_fma_f32 v[84:85], v[236:237], s[50:51], v[84:85] op_sel_hi:[1,0,1]
	v_pk_fma_f32 v[86:87], v[238:239], s[50:51], v[86:87] op_sel_hi:[1,0,1]
	v_pk_fma_f32 v[80:81], v[240:241], s[50:51], v[80:81] op_sel_hi:[1,0,1]
	v_pk_fma_f32 v[82:83], v[242:243], s[50:51], v[82:83] op_sel_hi:[1,0,1]
	v_cvt_pk_bf16_f32 v236, v84, v85
	v_cvt_pk_bf16_f32 v237, v86, v87
	v_cvt_pk_bf16_f32 v238, v80, v81
	v_cvt_pk_bf16_f32 v239, v82, v83
	s_add_u32 s100, s38, 0x90000
	s_addc_u32 s101, s39, 0
	global_store_dwordx4 v159, v[236:239], s[100:101]
	s_waitcnt vmcnt(9)
	v_sub_f32_e32 v244, v244, v154
	v_sub_f32_e32 v245, v245, v154
	v_sub_f32_e32 v246, v246, v154
	v_sub_f32_e32 v247, v247, v154
	v_sub_f32_e32 v248, v248, v154
	v_sub_f32_e32 v249, v249, v154
	v_sub_f32_e32 v250, v250, v154
	v_sub_f32_e32 v251, v251, v154
	v_pk_mul_f32 v[244:245], v[154:155], v[244:245] op_sel:[1,0]
	v_pk_mul_f32 v[246:247], v[154:155], v[246:247] op_sel:[1,0]
	v_pk_mul_f32 v[248:249], v[154:155], v[248:249] op_sel:[1,0]
	v_pk_mul_f32 v[250:251], v[154:155], v[250:251] op_sel:[1,0]
	v_pk_fma_f32 v[244:245], v[136:137], v[244:245], v[132:133]
	v_pk_fma_f32 v[246:247], v[138:139], v[246:247], v[134:135]
	v_pk_fma_f32 v[248:249], v[128:129], v[248:249], v[140:141]
	v_pk_fma_f32 v[250:251], v[130:131], v[250:251], v[142:143]
	v_pk_fma_f32 v[76:77], v[244:245], s[50:51], v[76:77] op_sel_hi:[1,0,1]
	v_pk_fma_f32 v[78:79], v[246:247], s[50:51], v[78:79] op_sel_hi:[1,0,1]
	v_pk_fma_f32 v[72:73], v[248:249], s[50:51], v[72:73] op_sel_hi:[1,0,1]
	v_pk_fma_f32 v[74:75], v[250:251], s[50:51], v[74:75] op_sel_hi:[1,0,1]
	v_cvt_pk_bf16_f32 v244, v76, v77
	v_cvt_pk_bf16_f32 v245, v78, v79
	v_cvt_pk_bf16_f32 v246, v72, v73
	v_cvt_pk_bf16_f32 v247, v74, v75
	s_add_u32 s100, s38, 0xa0000
	s_addc_u32 s101, s39, 0
	global_store_dwordx4 v159, v[244:247], s[100:101]
	s_waitcnt vmcnt(7)
; #define GAS __attribute__((address_space(1)))
; __device__ __forceinline__ v4u pack8(const f32x4 a, const f32x4 b) { v4u w; w.x = cvt_pk_bf16(a[0], a[1]); w.y = cvt_pk_bf16(a[2], a[3]); w.z = cvt_pk_bf16(b[0], b[1]); w.w = cvt_pk_bf16(b[2], b[3]); return w; }
; #define EPI_LOOP_AM for (int ai = 0; ai < 2; ++ai) _Pragma("unroll") for (int m = 0; m < 4; ++m)
;     __device__ __forceinline__ void operator()(Acc& acc, const Unit& u, LAS unsigned char*, int wr, int wc, int fr, int fq) const {
;     ...
;         for (int bj = 0; bj < 2; ++bj) { const int col = colb + bj * 128;
;             const f32x4 ga = *(const GAS f32x4*)(g0 + col), gb = *(const GAS f32x4*)(g0 + col + 4), ba = *(const GAS f32x4*)(b0 + col), bb = *(const GAS f32x4*)(b0 + col + 4);
; #pragma unroll
;             EPI_LOOP_AM { const int row = u.p0 * 256 + 128 * ai + 64 * wr + 16 * m + fr; const f32x2 st = *(const GAS f32x2*)(st0 + 2 * row); const size_t off = (size_t)row * D + col;
;                 const f32x4 xa = *(const GAS f32x4*)(x + off), xb = *(const GAS f32x4*)(x + off + 4);
;                 *(GAS v4u*)(z1 + off) = pack8(((xa - st.x) * st.y * ga + ba) * ALPHA + acc[ai][bj][m][0], ((xb - st.x) * st.y * gb + bb) * ALPHA + acc[ai][bj][m][1]); } }
	v_sub_f32_e32 v174, v174, v156
	v_sub_f32_e32 v175, v175, v156
	v_sub_f32_e32 v176, v176, v156
	v_sub_f32_e32 v177, v177, v156
	v_sub_f32_e32 v178, v178, v156
	v_sub_f32_e32 v179, v179, v156
	v_sub_f32_e32 v180, v180, v156
	v_sub_f32_e32 v181, v181, v156
	v_pk_mul_f32 v[174:175], v[156:157], v[174:175] op_sel:[1,0]
	v_pk_mul_f32 v[176:177], v[156:157], v[176:177] op_sel:[1,0]
	v_pk_mul_f32 v[178:179], v[156:157], v[178:179] op_sel:[1,0]
	v_pk_mul_f32 v[180:181], v[156:157], v[180:181] op_sel:[1,0]
	v_pk_fma_f32 v[174:175], v[136:137], v[174:175], v[132:133]
	v_pk_fma_f32 v[176:177], v[138:139], v[176:177], v[134:135]
	v_pk_fma_f32 v[178:179], v[128:129], v[178:179], v[140:141]
	v_pk_fma_f32 v[180:181], v[130:131], v[180:181], v[142:143]
	v_pk_fma_f32 v[64:65], v[174:175], s[50:51], v[64:65] op_sel_hi:[1,0,1]
	v_pk_fma_f32 v[66:67], v[176:177], s[50:51], v[66:67] op_sel_hi:[1,0,1]
	v_pk_fma_f32 v[56:57], v[178:179], s[50:51], v[56:57] op_sel_hi:[1,0,1]
	v_pk_fma_f32 v[58:59], v[180:181], s[50:51], v[58:59] op_sel_hi:[1,0,1]
	v_cvt_pk_bf16_f32 v174, v64, v65
	v_cvt_pk_bf16_f32 v175, v66, v67
	v_cvt_pk_bf16_f32 v176, v56, v57
	v_cvt_pk_bf16_f32 v177, v58, v59
	s_add_u32 s100, s38, 0xb0000
	s_addc_u32 s101, s39, 0
	global_store_dwordx4 v159, v[174:177], s[100:101]
	global_load_dwordx4 v[136:139], v161, s[14:15] offset:512
	global_load_dwordx4 v[128:131], v161, s[14:15] offset:528
	global_load_dwordx4 v[132:135], v161, s[16:17] offset:512
	global_load_dwordx4 v[140:143], v161, s[16:17] offset:528
	global_load_dwordx2 v[182:183], v160, s[40:41]
	global_load_dwordx4 v[196:199], v158, s[12:13] offset:512
	global_load_dwordx4 v[200:203], v158, s[12:13] offset:528
	s_add_u32 s98, s12, 0x20000
	s_addc_u32 s99, s13, 0
	global_load_dwordx2 v[184:185], v160, s[40:41] offset:128
	global_load_dwordx4 v[204:207], v158, s[98:99] offset:512
	global_load_dwordx4 v[208:211], v158, s[98:99] offset:528
	s_add_u32 s98, s12, 0x40000
	s_addc_u32 s99, s13, 0
	global_load_dwordx2 v[186:187], v160, s[40:41] offset:256
	global_load_dwordx4 v[212:215], v158, s[98:99] offset:512
	global_load_dwordx4 v[216:219], v158, s[98:99] offset:528
	s_add_u32 s98, s12, 0x60000
	s_addc_u32 s99, s13, 0
	global_load_dwordx2 v[148:149], v160, s[40:41] offset:384
	global_load_dwordx4 v[220:223], v158, s[98:99] offset:512
	global_load_dwordx4 v[224:227], v158, s[98:99] offset:528
	s_add_u32 s98, s12, 0x100000
	s_addc_u32 s99, s13, 0
	global_load_dwordx2 v[150:151], v160, s[40:41] offset:1024
	global_load_dwordx4 v[228:231], v158, s[98:99] offset:512
	global_load_dwordx4 v[232:235], v158, s[98:99] offset:528
	s_add_u32 s98, s12, 0x120000
	s_addc_u32 s99, s13, 0
	global_load_dwordx2 v[152:153], v160, s[40:41] offset:1152
	global_load_dwordx4 v[236:239], v158, s[98:99] offset:512
	global_load_dwordx4 v[240:243], v158, s[98:99] offset:528
	s_add_u32 s98, s12, 0x140000
	s_addc_u32 s99, s13, 0
	global_load_dwordx2 v[154:155], v160, s[40:41] offset:1280
	global_load_dwordx4 v[244:247], v158, s[98:99] offset:512
	global_load_dwordx4 v[248:251], v158, s[98:99] offset:528
	s_add_u32 s98, s12, 0x160000
	s_addc_u32 s99, s13, 0
	global_load_dwordx2 v[156:157], v160, s[40:41] offset:1408
	global_load_dwordx4 v[174:177], v158, s[98:99] offset:512
	global_load_dwordx4 v[178:181], v158, s[98:99] offset:528
	s_waitcnt vmcnt(21)
	v_sub_f32_e32 v196, v196, v182
	v_sub_f32_e32 v197, v197, v182
	v_sub_f32_e32 v198, v198, v182
	v_sub_f32_e32 v199, v199, v182
	v_sub_f32_e32 v200, v200, v182
	v_sub_f32_e32 v201, v201, v182
	v_sub_f32_e32 v202, v202, v182
	v_sub_f32_e32 v203, v203, v182
	v_pk_mul_f32 v[196:197], v[182:183], v[196:197] op_sel:[1,0]
	v_pk_mul_f32 v[198:199], v[182:183], v[198:199] op_sel:[1,0]
	v_pk_mul_f32 v[200:201], v[182:183], v[200:201] op_sel:[1,0]
	v_pk_mul_f32 v[202:203], v[182:183], v[202:203] op_sel:[1,0]
	v_pk_fma_f32 v[196:197], v[136:137], v[196:197], v[132:133]
	v_pk_fma_f32 v[198:199], v[138:139], v[198:199], v[134:135]
	v_pk_fma_f32 v[200:201], v[128:129], v[200:201], v[140:141]
	v_pk_fma_f32 v[202:203], v[130:131], v[202:203], v[142:143]
	v_pk_fma_f32 v[68:69], v[196:197], s[50:51], v[68:69] op_sel_hi:[1,0,1]
	v_pk_fma_f32 v[70:71], v[198:199], s[50:51], v[70:71] op_sel_hi:[1,0,1]
	v_pk_fma_f32 v[60:61], v[200:201], s[50:51], v[60:61] op_sel_hi:[1,0,1]
	v_pk_fma_f32 v[62:63], v[202:203], s[50:51], v[62:63] op_sel_hi:[1,0,1]
	v_cvt_pk_bf16_f32 v196, v68, v69
	v_cvt_pk_bf16_f32 v197, v70, v71
	v_cvt_pk_bf16_f32 v198, v60, v61
	v_cvt_pk_bf16_f32 v199, v62, v63
	global_store_dwordx4 v159, v[196:199], s[38:39] offset:256
	s_waitcnt vmcnt(19)
	v_sub_f32_e32 v204, v204, v184
	v_sub_f32_e32 v205, v205, v184
	v_sub_f32_e32 v206, v206, v184
	v_sub_f32_e32 v207, v207, v184
	v_sub_f32_e32 v208, v208, v184
	v_sub_f32_e32 v209, v209, v184
	v_sub_f32_e32 v210, v210, v184
	v_sub_f32_e32 v211, v211, v184
	v_pk_mul_f32 v[204:205], v[184:185], v[204:205] op_sel:[1,0]
	v_pk_mul_f32 v[206:207], v[184:185], v[206:207] op_sel:[1,0]
	v_pk_mul_f32 v[208:209], v[184:185], v[208:209] op_sel:[1,0]
	v_pk_mul_f32 v[210:211], v[184:185], v[210:211] op_sel:[1,0]
	v_pk_fma_f32 v[204:205], v[136:137], v[204:205], v[132:133]
	v_pk_fma_f32 v[206:207], v[138:139], v[206:207], v[134:135]
	v_pk_fma_f32 v[208:209], v[128:129], v[208:209], v[140:141]
	v_pk_fma_f32 v[210:211], v[130:131], v[210:211], v[142:143]
	v_pk_fma_f32 v[52:53], v[204:205], s[50:51], v[52:53] op_sel_hi:[1,0,1]
	v_pk_fma_f32 v[54:55], v[206:207], s[50:51], v[54:55] op_sel_hi:[1,0,1]
	v_pk_fma_f32 v[48:49], v[208:209], s[50:51], v[48:49] op_sel_hi:[1,0,1]
	v_pk_fma_f32 v[50:51], v[210:211], s[50:51], v[50:51] op_sel_hi:[1,0,1]
	v_cvt_pk_bf16_f32 v204, v52, v53
	v_cvt_pk_bf16_f32 v205, v54, v55
	v_cvt_pk_bf16_f32 v206, v48, v49
	v_cvt_pk_bf16_f32 v207, v50, v51
	s_add_u32 s100, s38, 0x10000
	s_addc_u32 s101, s39, 0
	global_store_dwordx4 v159, v[204:207], s[100:101] offset:256
	s_waitcnt vmcnt(17)
; #define GAS __attribute__((address_space(1)))
; __device__ __forceinline__ v4u pack8(const f32x4 a, const f32x4 b) { v4u w; w.x = cvt_pk_bf16(a[0], a[1]); w.y = cvt_pk_bf16(a[2], a[3]); w.z = cvt_pk_bf16(b[0], b[1]); w.w = cvt_pk_bf16(b[2], b[3]); return w; }
; #define EPI_LOOP_AM for (int ai = 0; ai < 2; ++ai) _Pragma("unroll") for (int m = 0; m < 4; ++m)
;     __device__ __forceinline__ void operator()(Acc& acc, const Unit& u, LAS unsigned char*, int wr, int wc, int fr, int fq) const {
;     ...
;             const f32x4 ga = *(const GAS f32x4*)(g0 + col), gb = *(const GAS f32x4*)(g0 + col + 4), ba = *(const GAS f32x4*)(b0 + col), bb = *(const GAS f32x4*)(b0 + col + 4);
; #pragma unroll
;             EPI_LOOP_AM { const int row = u.p0 * 256 + 128 * ai + 64 * wr + 16 * m + fr; const f32x2 st = *(const GAS f32x2*)(st0 + 2 * row); const size_t off = (size_t)row * D + col;
;                 const f32x4 xa = *(const GAS f32x4*)(x + off), xb = *(const GAS f32x4*)(x + off + 4);
;                 *(GAS v4u*)(z1 + off) = pack8(((xa - st.x) * st.y * ga + ba) * ALPHA + acc[ai][bj][m][0], ((xb - st.x) * st.y * gb + bb) * ALPHA + acc[ai][bj][m][1]); } }
	v_sub_f32_e32 v212, v212, v186
	v_sub_f32_e32 v213, v213, v186
	v_sub_f32_e32 v214, v214, v186
	v_sub_f32_e32 v215, v215, v186
	v_sub_f32_e32 v216, v216, v186
	v_sub_f32_e32 v217, v217, v186
	v_sub_f32_e32 v218, v218, v186
	v_sub_f32_e32 v219, v219, v186
	v_pk_mul_f32 v[212:213], v[186:187], v[212:213] op_sel:[1,0]
	v_pk_mul_f32 v[214:215], v[186:187], v[214:215] op_sel:[1,0]
	v_pk_mul_f32 v[216:217], v[186:187], v[216:217] op_sel:[1,0]
	v_pk_mul_f32 v[218:219], v[186:187], v[218:219] op_sel:[1,0]
	v_pk_fma_f32 v[212:213], v[136:137], v[212:213], v[132:133]
	v_pk_fma_f32 v[214:215], v[138:139], v[214:215], v[134:135]
	v_pk_fma_f32 v[216:217], v[128:129], v[216:217], v[140:141]
	v_pk_fma_f32 v[218:219], v[130:131], v[218:219], v[142:143]
	v_pk_fma_f32 v[44:45], v[212:213], s[50:51], v[44:45] op_sel_hi:[1,0,1]
	v_pk_fma_f32 v[46:47], v[214:215], s[50:51], v[46:47] op_sel_hi:[1,0,1]
	v_pk_fma_f32 v[40:41], v[216:217], s[50:51], v[40:41] op_sel_hi:[1,0,1]
	v_pk_fma_f32 v[42:43], v[218:219], s[50:51], v[42:43] op_sel_hi:[1,0,1]
	v_cvt_pk_bf16_f32 v212, v44, v45
	v_cvt_pk_bf16_f32 v213, v46, v47
	v_cvt_pk_bf16_f32 v214, v40, v41
	v_cvt_pk_bf16_f32 v215, v42, v43
	s_add_u32 s100, s38, 0x20000
	s_addc_u32 s101, s39, 0
	global_store_dwordx4 v159, v[212:215], s[100:101] offset:256
	s_waitcnt vmcnt(15)
	v_sub_f32_e32 v220, v220, v148
	v_sub_f32_e32 v221, v221, v148
	v_sub_f32_e32 v222, v222, v148
	v_sub_f32_e32 v223, v223, v148
	v_sub_f32_e32 v224, v224, v148
	v_sub_f32_e32 v225, v225, v148
	v_sub_f32_e32 v226, v226, v148
	v_sub_f32_e32 v227, v227, v148
	v_pk_mul_f32 v[220:221], v[148:149], v[220:221] op_sel:[1,0]
	v_pk_mul_f32 v[222:223], v[148:149], v[222:223] op_sel:[1,0]
	v_pk_mul_f32 v[224:225], v[148:149], v[224:225] op_sel:[1,0]
	v_pk_mul_f32 v[226:227], v[148:149], v[226:227] op_sel:[1,0]
	v_pk_fma_f32 v[220:221], v[136:137], v[220:221], v[132:133]
	v_pk_fma_f32 v[222:223], v[138:139], v[222:223], v[134:135]
	v_pk_fma_f32 v[224:225], v[128:129], v[224:225], v[140:141]
	v_pk_fma_f32 v[226:227], v[130:131], v[226:227], v[142:143]
	v_pk_fma_f32 v[36:37], v[220:221], s[50:51], v[36:37] op_sel_hi:[1,0,1]
	v_pk_fma_f32 v[38:39], v[222:223], s[50:51], v[38:39] op_sel_hi:[1,0,1]
	v_pk_fma_f32 v[32:33], v[224:225], s[50:51], v[32:33] op_sel_hi:[1,0,1]
	v_pk_fma_f32 v[34:35], v[226:227], s[50:51], v[34:35] op_sel_hi:[1,0,1]
	v_cvt_pk_bf16_f32 v220, v36, v37
	v_cvt_pk_bf16_f32 v221, v38, v39
	v_cvt_pk_bf16_f32 v222, v32, v33
	v_cvt_pk_bf16_f32 v223, v34, v35
	s_add_u32 s100, s38, 0x30000
	s_addc_u32 s101, s39, 0
	global_store_dwordx4 v159, v[220:223], s[100:101] offset:256
	s_waitcnt vmcnt(13)
	v_sub_f32_e32 v228, v228, v150
	v_sub_f32_e32 v229, v229, v150
	v_sub_f32_e32 v230, v230, v150
	v_sub_f32_e32 v231, v231, v150
	v_sub_f32_e32 v232, v232, v150
	v_sub_f32_e32 v233, v233, v150
	v_sub_f32_e32 v234, v234, v150
	v_sub_f32_e32 v235, v235, v150
	v_pk_mul_f32 v[228:229], v[150:151], v[228:229] op_sel:[1,0]
	v_pk_mul_f32 v[230:231], v[150:151], v[230:231] op_sel:[1,0]
	v_pk_mul_f32 v[232:233], v[150:151], v[232:233] op_sel:[1,0]
	v_pk_mul_f32 v[234:235], v[150:151], v[234:235] op_sel:[1,0]
	v_pk_fma_f32 v[228:229], v[136:137], v[228:229], v[132:133]
	v_pk_fma_f32 v[230:231], v[138:139], v[230:231], v[134:135]
	v_pk_fma_f32 v[232:233], v[128:129], v[232:233], v[140:141]
	v_pk_fma_f32 v[234:235], v[130:131], v[234:235], v[142:143]
	v_pk_fma_f32 v[28:29], v[228:229], s[50:51], v[28:29] op_sel_hi:[1,0,1]
	v_pk_fma_f32 v[30:31], v[230:231], s[50:51], v[30:31] op_sel_hi:[1,0,1]
	v_pk_fma_f32 v[24:25], v[232:233], s[50:51], v[24:25] op_sel_hi:[1,0,1]
	v_pk_fma_f32 v[26:27], v[234:235], s[50:51], v[26:27] op_sel_hi:[1,0,1]
	v_cvt_pk_bf16_f32 v228, v28, v29
	v_cvt_pk_bf16_f32 v229, v30, v31
	v_cvt_pk_bf16_f32 v230, v24, v25
	v_cvt_pk_bf16_f32 v231, v26, v27
	s_add_u32 s100, s38, 0x80000
	s_addc_u32 s101, s39, 0
	global_store_dwordx4 v159, v[228:231], s[100:101] offset:256
	s_waitcnt vmcnt(11)
; #define GAS __attribute__((address_space(1)))
; __device__ __forceinline__ v4u pack8(const f32x4 a, const f32x4 b) { v4u w; w.x = cvt_pk_bf16(a[0], a[1]); w.y = cvt_pk_bf16(a[2], a[3]); w.z = cvt_pk_bf16(b[0], b[1]); w.w = cvt_pk_bf16(b[2], b[3]); return w; }
; #define EPI_LOOP_AM for (int ai = 0; ai < 2; ++ai) _Pragma("unroll") for (int m = 0; m < 4; ++m)
;     __device__ __forceinline__ void operator()(Acc& acc, const Unit& u, LAS unsigned char*, int wr, int wc, int fr, int fq) const {
;     ...
;         for (int bj = 0; bj < 2; ++bj) { const int col = colb + bj * 128;
;             const f32x4 ga = *(const GAS f32x4*)(g0 + col), gb = *(const GAS f32x4*)(g0 + col + 4), ba = *(const GAS f32x4*)(b0 + col), bb = *(const GAS f32x4*)(b0 + col + 4);
; #pragma unroll
;             EPI_LOOP_AM { const int row = u.p0 * 256 + 128 * ai + 64 * wr + 16 * m + fr; const f32x2 st = *(const GAS f32x2*)(st0 + 2 * row); const size_t off = (size_t)row * D + col;
;                 const f32x4 xa = *(const GAS f32x4*)(x + off), xb = *(const GAS f32x4*)(x + off + 4);
;                 *(GAS v4u*)(z1 + off) = pack8(((xa - st.x) * st.y * ga + ba) * ALPHA + acc[ai][bj][m][0], ((xb - st.x) * st.y * gb + bb) * ALPHA + acc[ai][bj][m][1]); } }
	v_sub_f32_e32 v236, v236, v152
	v_sub_f32_e32 v237, v237, v152
	v_sub_f32_e32 v238, v238, v152
	v_sub_f32_e32 v239, v239, v152
	v_sub_f32_e32 v240, v240, v152
	v_sub_f32_e32 v241, v241, v152
	v_sub_f32_e32 v242, v242, v152
	v_sub_f32_e32 v243, v243, v152
	v_pk_mul_f32 v[236:237], v[152:153], v[236:237] op_sel:[1,0]
	v_pk_mul_f32 v[238:239], v[152:153], v[238:239] op_sel:[1,0]
	v_pk_mul_f32 v[240:241], v[152:153], v[240:241] op_sel:[1,0]
	v_pk_mul_f32 v[242:243], v[152:153], v[242:243] op_sel:[1,0]
	v_pk_fma_f32 v[236:237], v[136:137], v[236:237], v[132:133]
	v_pk_fma_f32 v[238:239], v[138:139], v[238:239], v[134:135]
	v_pk_fma_f32 v[240:241], v[128:129], v[240:241], v[140:141]
	v_pk_fma_f32 v[242:243], v[130:131], v[242:243], v[142:143]
	v_pk_fma_f32 v[20:21], v[236:237], s[50:51], v[20:21] op_sel_hi:[1,0,1]
	v_pk_fma_f32 v[22:23], v[238:239], s[50:51], v[22:23] op_sel_hi:[1,0,1]
	v_pk_fma_f32 v[16:17], v[240:241], s[50:51], v[16:17] op_sel_hi:[1,0,1]
	v_pk_fma_f32 v[18:19], v[242:243], s[50:51], v[18:19] op_sel_hi:[1,0,1]
	v_cvt_pk_bf16_f32 v236, v20, v21
	v_cvt_pk_bf16_f32 v237, v22, v23
	v_cvt_pk_bf16_f32 v238, v16, v17
	v_cvt_pk_bf16_f32 v239, v18, v19
	s_add_u32 s100, s38, 0x90000
	s_addc_u32 s101, s39, 0
	global_store_dwordx4 v159, v[236:239], s[100:101] offset:256
	s_waitcnt vmcnt(9)
	v_sub_f32_e32 v244, v244, v154
	v_sub_f32_e32 v245, v245, v154
	v_sub_f32_e32 v246, v246, v154
	v_sub_f32_e32 v247, v247, v154
	v_sub_f32_e32 v248, v248, v154
	v_sub_f32_e32 v249, v249, v154
	v_sub_f32_e32 v250, v250, v154
	v_sub_f32_e32 v251, v251, v154
	v_pk_mul_f32 v[244:245], v[154:155], v[244:245] op_sel:[1,0]
	v_pk_mul_f32 v[246:247], v[154:155], v[246:247] op_sel:[1,0]
	v_pk_mul_f32 v[248:249], v[154:155], v[248:249] op_sel:[1,0]
	v_pk_mul_f32 v[250:251], v[154:155], v[250:251] op_sel:[1,0]
	v_pk_fma_f32 v[244:245], v[136:137], v[244:245], v[132:133]
	v_pk_fma_f32 v[246:247], v[138:139], v[246:247], v[134:135]
	v_pk_fma_f32 v[248:249], v[128:129], v[248:249], v[140:141]
	v_pk_fma_f32 v[250:251], v[130:131], v[250:251], v[142:143]
	v_pk_fma_f32 v[12:13], v[244:245], s[50:51], v[12:13] op_sel_hi:[1,0,1]
	v_pk_fma_f32 v[14:15], v[246:247], s[50:51], v[14:15] op_sel_hi:[1,0,1]
	v_pk_fma_f32 v[8:9], v[248:249], s[50:51], v[8:9] op_sel_hi:[1,0,1]
	v_pk_fma_f32 v[10:11], v[250:251], s[50:51], v[10:11] op_sel_hi:[1,0,1]
	v_cvt_pk_bf16_f32 v244, v12, v13
	v_cvt_pk_bf16_f32 v245, v14, v15
	v_cvt_pk_bf16_f32 v246, v8, v9
	v_cvt_pk_bf16_f32 v247, v10, v11
	s_add_u32 s100, s38, 0xa0000
	s_addc_u32 s101, s39, 0
	global_store_dwordx4 v159, v[244:247], s[100:101] offset:256
	s_waitcnt vmcnt(7)
	v_sub_f32_e32 v174, v174, v156
	v_sub_f32_e32 v175, v175, v156
	v_sub_f32_e32 v176, v176, v156
	v_sub_f32_e32 v177, v177, v156
	v_sub_f32_e32 v178, v178, v156
	v_sub_f32_e32 v179, v179, v156
	v_sub_f32_e32 v180, v180, v156
	v_sub_f32_e32 v181, v181, v156
	v_pk_mul_f32 v[174:175], v[156:157], v[174:175] op_sel:[1,0]
	v_pk_mul_f32 v[176:177], v[156:157], v[176:177] op_sel:[1,0]
	v_pk_mul_f32 v[178:179], v[156:157], v[178:179] op_sel:[1,0]
	v_pk_mul_f32 v[180:181], v[156:157], v[180:181] op_sel:[1,0]
	v_pk_fma_f32 v[174:175], v[136:137], v[174:175], v[132:133]
	v_pk_fma_f32 v[176:177], v[138:139], v[176:177], v[134:135]
	v_pk_fma_f32 v[178:179], v[128:129], v[178:179], v[140:141]
	v_pk_fma_f32 v[180:181], v[130:131], v[180:181], v[142:143]
	v_pk_fma_f32 v[4:5], v[174:175], s[50:51], v[4:5] op_sel_hi:[1,0,1]
	v_pk_fma_f32 v[6:7], v[176:177], s[50:51], v[6:7] op_sel_hi:[1,0,1]
	v_pk_fma_f32 v[0:1], v[178:179], s[50:51], v[0:1] op_sel_hi:[1,0,1]
	v_pk_fma_f32 v[2:3], v[180:181], s[50:51], v[2:3] op_sel_hi:[1,0,1]
	v_cvt_pk_bf16_f32 v174, v4, v5
	v_cvt_pk_bf16_f32 v175, v6, v7
	v_cvt_pk_bf16_f32 v176, v0, v1
	v_cvt_pk_bf16_f32 v177, v2, v3
	s_add_u32 s100, s38, 0xb0000
	s_addc_u32 s101, s39, 0
	global_store_dwordx4 v159, v[174:177], s[100:101] offset:256
	s_cbranch_vccnz .LBB0_1310
	s_and_b64 vcc, exec, s[4:5]
	s_cbranch_vccnz .LBB0_1309
	s_barrier
	s_branch .LBB0_1309

; #define LAS __attribute__((address_space(3)))
; __global__ void __launch_bounds__(NTHR, 2) fwd(Args args) {
;     extern __shared__ __attribute__((aligned(16))) unsigned char lds_raw[];
;     Frame F;
;     F.lds = (LAS unsigned char*)lds_raw; F.ws = args.ws; F.ctl = (unsigned*)(args.ws + WS_CTL);
;     F.wave = __builtin_amdgcn_readfirstlane((int)threadIdx.x >> 6);
;     F.G = gridDim.x; { const int bx = blockIdx.x; F.vcu = (F.G % 8 == 0) ? (bx % 8) * (F.G / 8) + bx / 8 : bx; }
	.amdhsa_kernel _Z3fwd4Args
		.amdhsa_group_segment_fixed_size 0
		.amdhsa_private_segment_fixed_size 0
		.amdhsa_kernarg_size 424
		.amdhsa_user_sgpr_count 2
		.amdhsa_user_sgpr_dispatch_ptr 0
		.amdhsa_user_sgpr_queue_ptr 0
		.amdhsa_user_sgpr_kernarg_segment_ptr 1
		.amdhsa_user_sgpr_dispatch_id 0
		.amdhsa_user_sgpr_kernarg_preload_length 0
		.amdhsa_user_sgpr_kernarg_preload_offset 0
		.amdhsa_user_sgpr_private_segment_size 0
		.amdhsa_uses_dynamic_stack 0
		.amdhsa_enable_private_segment 0
		.amdhsa_system_sgpr_workgroup_id_x 1
		.amdhsa_system_sgpr_workgroup_id_y 0
		.amdhsa_system_sgpr_workgroup_id_z 0
		.amdhsa_system_sgpr_workgroup_info 0
		.amdhsa_system_vgpr_workitem_id 0
		.amdhsa_next_free_vgpr 256
		.amdhsa_next_free_sgpr 102
		.amdhsa_accum_offset 256
		.amdhsa_reserve_vcc 1
		.amdhsa_float_round_mode_32 0
		.amdhsa_float_round_mode_16_64 0
		.amdhsa_float_denorm_mode_32 3
		.amdhsa_float_denorm_mode_16_64 3
		.amdhsa_dx10_clamp 1
		.amdhsa_ieee_mode 1
		.amdhsa_fp16_overflow 0
		.amdhsa_tg_split 0
		.amdhsa_exception_fp_ieee_invalid_op 0
		.amdhsa_exception_fp_denorm_src 0
		.amdhsa_exception_fp_ieee_div_zero 0
		.amdhsa_exception_fp_ieee_overflow 0
		.amdhsa_exception_fp_ieee_underflow 0
		.amdhsa_exception_fp_ieee_inexact 0
		.amdhsa_exception_int_div_zero 0
	.end_amdhsa_kernel

; #define LAS __attribute__((address_space(3)))
; __global__ void __launch_bounds__(NTHR, 2) fwd(Args args) {
;     extern __shared__ __attribute__((aligned(16))) unsigned char lds_raw[];
;     Frame F;
;     F.lds = (LAS unsigned char*)lds_raw; F.ws = args.ws; F.ctl = (unsigned*)(args.ws + WS_CTL);
;     F.wave = __builtin_amdgcn_readfirstlane((int)threadIdx.x >> 6);
;     F.G = gridDim.x; { const int bx = blockIdx.x; F.vcu = (F.G % 8 == 0) ? (bx % 8) * (F.G / 8) + bx / 8 : bx; }
amdhsa.kernels:
  - .agpr_count:     0
    .args:
      - .offset:         0
        .size:           168
        .value_kind:     by_value
      - .offset:         168
        .size:           4
        .value_kind:     hidden_block_count_x
      - .offset:         172
        .size:           4
        .value_kind:     hidden_block_count_y
      - .offset:         176
        .size:           4
        .value_kind:     hidden_block_count_z
      - .offset:         180
        .size:           2
        .value_kind:     hidden_group_size_x
      - .offset:         182
        .size:           2
        .value_kind:     hidden_group_size_y
      - .offset:         184
        .size:           2
        .value_kind:     hidden_group_size_z
      - .offset:         186
        .size:           2
        .value_kind:     hidden_remainder_x
      - .offset:         188
        .size:           2
        .value_kind:     hidden_remainder_y
      - .offset:         190
        .size:           2
        .value_kind:     hidden_remainder_z
      - .offset:         208
        .size:           8
        .value_kind:     hidden_global_offset_x
      - .offset:         216
        .size:           8
        .value_kind:     hidden_global_offset_y
      - .offset:         224
        .size:           8
        .value_kind:     hidden_global_offset_z
      - .offset:         232
        .size:           2
        .value_kind:     hidden_grid_dims
      - .offset:         288
        .size:           4
        .value_kind:     hidden_dynamic_lds_size
    .group_segment_fixed_size: 0
    .kernarg_segment_align: 8
    .kernarg_segment_size: 424
    .language:       OpenCL C
    .language_version:
      - 2
      - 0
    .max_flat_workgroup_size: 512
    .name:           _Z3fwd4Args
    .private_segment_fixed_size: 0
    .sgpr_count:     108
    .sgpr_spill_count: 92
    .symbol:         _Z3fwd4Args.kd
    .uniform_work_group_size: 1
    .uses_dynamic_stack: false
    .vgpr_count:     256
    .vgpr_spill_count: 0
    .wavefront_size: 64
